# combine phase (layer 0): next-layer norm gain/scale/shift loads hoisted above the row reduction with counted vmcnt (was a 4x load-wait-store ladder); attention ring+remap dropped (neutral)
# baseline (speedup 1.0000x reference)
; __device__ __forceinline__ unsigned pk2(float lo, float hi) { return f2bf(lo) | (f2bf(hi) << 16); }
; __device__ __forceinline__ float wave_sum(float v) {
; #pragma unroll
;     for (int o = 1; o < 64; o <<= 1) v += __shfl_xor(v, o);
;     return v;
; __device__ __forceinline__ void phase_combine(const Args& a, const Ctx& c0, int l, bool last_in) {
;     ...
;         if (!last) {
;             const float* mv1 = modv + (size_t)5 * NMODW + (size_t)mb * NMODW; const float* g1n = INP(6) + (size_t)(l + 1) * DM;
;             const float rstd = rsqrtf(wave_sum(ssn) * (1.f / DM) + EPS); bf16* hrow = WSP(bf16, WS_H) + (size_t)row * DM;
; #pragma unroll
;             for (int j = 0; j < 4; ++j) { const int idx = (lane + 64 * j) * 8; u32x4 w;
; #pragma unroll
;                 for (int hlf = 0; hlf < 2; ++hlf) { const int ix = idx + hlf * 4; const f32x4 gsv = *(const f32x4*)(g1n + ix) * (1.f + *(const f32x4*)(mv1 + DM + ix)), shv = *(const f32x4*)(mv1 + ix);
;                     const f32x4 o = (xv[j][hlf] * rstd) * gsv + shv;
;                     if (hlf == 0) { w.x = pk2(o.x, o.y); w.y = pk2(o.z, o.w); } else { w.z = pk2(o.x, o.y); w.w = pk2(o.z, o.w); } }
;                 *(u32x4*)(hrow + idx) = w; } }
.LBB0_2751:
	s_add_u32 s2, s36, s16
	s_addc_u32 s3, s40, s17
	s_add_u32 s16, s2, 0x2000
	s_addc_u32 s17, s3, 0
	global_load_dwordx4 v[136:139], v57, s[2:3] offset:16
	global_load_dwordx4 v[140:143], v57, s[2:3]
	global_load_dwordx4 v[148:151], v[60:61], off offset:16
	global_load_dwordx4 v[152:155], v[60:61], off
	global_load_dwordx4 v[156:159], v57, s[16:17] offset:16
	global_load_dwordx4 v[160:163], v57, s[16:17]
	global_load_dwordx4 v[164:167], v57, s[2:3] offset:2064
	global_load_dwordx4 v[168:171], v57, s[2:3] offset:2048
	global_load_dwordx4 v[172:175], v[62:63], off offset:16
	global_load_dwordx4 v[176:179], v[62:63], off
	global_load_dwordx4 v[184:187], v104, s[16:17] offset:16
	global_load_dwordx4 v[188:191], v104, s[16:17]
	global_load_dwordx4 v[192:195], v105, s[2:3] offset:16
	global_load_dwordx4 v[196:199], v105, s[2:3]
	global_load_dwordx4 v[200:203], v[64:65], off offset:16
	global_load_dwordx4 v[204:207], v[64:65], off
	global_load_dwordx4 v[240:243], v105, s[16:17] offset:16
	global_load_dwordx4 v[244:247], v105, s[16:17]
	v_mul_f32_e32 v1, v39, v39
	v_mul_f32_e32 v18, v41, v41
	v_fmac_f32_e32 v1, v38, v38
	v_fmac_f32_e32 v18, v40, v40
	v_add_f32_e32 v1, v1, v18
	v_mul_f32_e32 v18, v35, v35
	v_mul_f32_e32 v19, v37, v37
	v_fmac_f32_e32 v18, v34, v34
	v_fmac_f32_e32 v19, v36, v36
	v_add_f32_e32 v18, v18, v19
	v_add_f32_e32 v1, v18, v1
	v_mul_f32_e32 v18, v31, v31
	v_mul_f32_e32 v19, v33, v33
	v_fmac_f32_e32 v18, v30, v30
	v_fmac_f32_e32 v19, v32, v32
	v_add_f32_e32 v18, v18, v19
	v_add_f32_e32 v1, v18, v1
	v_mul_f32_e32 v18, v23, v23
	v_mul_f32_e32 v19, v25, v25
	v_fmac_f32_e32 v18, v22, v22
	v_fmac_f32_e32 v19, v24, v24
	v_add_f32_e32 v18, v18, v19
	v_add_f32_e32 v1, v18, v1
	v_mul_f32_e32 v18, v15, v15
	v_mul_f32_e32 v19, v17, v17
	v_fmac_f32_e32 v18, v14, v14
	v_fmac_f32_e32 v19, v16, v16
	v_add_f32_e32 v18, v18, v19
	v_add_f32_e32 v1, v18, v1
	v_mul_f32_e32 v18, v11, v11
	v_mul_f32_e32 v19, v13, v13
	v_fmac_f32_e32 v18, v10, v10
	v_fmac_f32_e32 v19, v12, v12
	v_add_f32_e32 v18, v18, v19
	v_add_f32_e32 v1, v18, v1
	v_mul_f32_e32 v18, v7, v7
	v_mul_f32_e32 v19, v9, v9
	v_fmac_f32_e32 v18, v6, v6
	v_fmac_f32_e32 v19, v8, v8
	v_add_f32_e32 v18, v18, v19
	v_add_f32_e32 v1, v18, v1
	v_mul_f32_e32 v18, v3, v3
	v_mul_f32_e32 v19, v5, v5
	v_fmac_f32_e32 v18, v2, v2
	v_fmac_f32_e32 v19, v4, v4
	v_add_f32_e32 v18, v18, v19
	v_add_f32_e32 v1, v18, v1
	v_xor_b32_e32 v18, 1, v210
	v_cmp_lt_i32_e32 vcc, v18, v215
	s_nop 1
	v_cndmask_b32_e32 v18, v210, v18, vcc
	v_lshlrev_b32_e32 v18, 2, v18
	ds_bpermute_b32 v18, v18, v1
	s_waitcnt lgkmcnt(0)
	v_add_f32_e32 v1, v1, v18
	v_xor_b32_e32 v18, 2, v210
	v_cmp_lt_i32_e32 vcc, v18, v215
	s_nop 1
	v_cndmask_b32_e32 v18, v210, v18, vcc
	v_lshlrev_b32_e32 v18, 2, v18
	ds_bpermute_b32 v18, v18, v1
	s_waitcnt lgkmcnt(0)
	v_add_f32_e32 v1, v1, v18
	v_xor_b32_e32 v18, 4, v210
	v_cmp_lt_i32_e32 vcc, v18, v215
	s_nop 1
	v_cndmask_b32_e32 v18, v210, v18, vcc
	v_lshlrev_b32_e32 v18, 2, v18
	ds_bpermute_b32 v18, v18, v1
	s_waitcnt lgkmcnt(0)
	v_add_f32_e32 v1, v1, v18
	v_xor_b32_e32 v18, 8, v210
	v_cmp_lt_i32_e32 vcc, v18, v215
	s_nop 1
	v_cndmask_b32_e32 v18, v210, v18, vcc
	v_lshlrev_b32_e32 v18, 2, v18
	ds_bpermute_b32 v18, v18, v1
	v_cmp_lt_i32_e32 vcc, v220, v215
	s_waitcnt lgkmcnt(0)
	v_add_f32_e32 v1, v1, v18
	v_cndmask_b32_e32 v18, v210, v220, vcc
	v_lshlrev_b32_e32 v18, 2, v18
	ds_bpermute_b32 v18, v18, v1
	v_cmp_lt_i32_e32 vcc, v221, v215
	s_waitcnt lgkmcnt(0)
	v_add_f32_e32 v1, v1, v18
	v_cndmask_b32_e32 v18, v210, v221, vcc
	v_lshlrev_b32_e32 v18, 2, v18
	ds_bpermute_b32 v18, v18, v1
	s_waitcnt lgkmcnt(0)
	v_add_f32_e32 v1, v1, v18
	v_fmamk_f32 v1, v1, 0x3a000000, v180
	v_cmp_gt_f32_e32 vcc, s79, v1
	v_mul_f32_e32 v18, 0x4b800000, v1
	s_nop 0
	v_cndmask_b32_e32 v1, v1, v18, vcc
	v_rsq_f32_e32 v1, v1
	s_nop 0
	v_mul_f32_e32 v18, 0x45800000, v1
	v_cndmask_b32_e32 v72, v1, v18, vcc
	v_pk_mul_f32 v[38:39], v[38:39], v[72:73] op_sel_hi:[1,0]
	v_pk_mul_f32 v[40:41], v[40:41], v[72:73] op_sel_hi:[1,0]
	v_pk_mul_f32 v[34:35], v[34:35], v[72:73] op_sel_hi:[1,0]
	v_pk_mul_f32 v[36:37], v[36:37], v[72:73] op_sel_hi:[1,0]
	v_pk_mul_f32 v[30:31], v[30:31], v[72:73] op_sel_hi:[1,0]
	v_pk_mul_f32 v[32:33], v[32:33], v[72:73] op_sel_hi:[1,0]
	v_pk_mul_f32 v[22:23], v[22:23], v[72:73] op_sel_hi:[1,0]
	v_pk_mul_f32 v[24:25], v[24:25], v[72:73] op_sel_hi:[1,0]
	v_pk_mul_f32 v[14:15], v[14:15], v[72:73] op_sel_hi:[1,0]
	v_pk_mul_f32 v[16:17], v[16:17], v[72:73] op_sel_hi:[1,0]
	v_pk_mul_f32 v[10:11], v[10:11], v[72:73] op_sel_hi:[1,0]
	v_pk_mul_f32 v[12:13], v[12:13], v[72:73] op_sel_hi:[1,0]
	v_pk_mul_f32 v[6:7], v[6:7], v[72:73] op_sel_hi:[1,0]
	v_pk_mul_f32 v[8:9], v[8:9], v[72:73] op_sel_hi:[1,0]
	v_pk_mul_f32 v[2:3], v[2:3], v[72:73] op_sel_hi:[1,0]
	v_pk_mul_f32 v[4:5], v[4:5], v[72:73] op_sel_hi:[1,0]
	s_waitcnt vmcnt(12)
; __device__ __forceinline__ unsigned pk2(float lo, float hi) { return f2bf(lo) | (f2bf(hi) << 16); }
; __device__ __forceinline__ void phase_combine(const Args& a, const Ctx& c0, int l, bool last_in) {
;     ...
; #pragma unroll
;             for (int j = 0; j < 4; ++j) { const int idx = (lane + 64 * j) * 8; u32x4 w;
; #pragma unroll
;                 for (int hlf = 0; hlf < 2; ++hlf) { const int ix = idx + hlf * 4; const f32x4 gsv = *(const f32x4*)(g1n + ix) * (1.f + *(const f32x4*)(mv1 + DM + ix)), shv = *(const f32x4*)(mv1 + ix);
;                     const f32x4 o = (xv[j][hlf] * rstd) * gsv + shv;
;                     if (hlf == 0) { w.x = pk2(o.x, o.y); w.y = pk2(o.z, o.w); } else { w.z = pk2(o.x, o.y); w.w = pk2(o.z, o.w); } }
;                 *(u32x4*)(hrow + idx) = w; } }
	v_pk_add_f32 v[42:43], v[156:157], 1.0 op_sel_hi:[1,0]
	v_pk_add_f32 v[74:75], v[160:161], 1.0 op_sel_hi:[1,0]
	v_pk_add_f32 v[76:77], v[162:163], 1.0 op_sel_hi:[1,0]
	v_pk_mul_f32 v[50:51], v[152:153], v[74:75]
	v_pk_mul_f32 v[52:53], v[154:155], v[76:77]
	v_pk_fma_f32 v[38:39], v[50:51], v[38:39], v[140:141]
	v_pk_fma_f32 v[40:41], v[52:53], v[40:41], v[142:143]
	v_bfe_u32 v1, v38, 16, 1
	v_add3_u32 v1, v38, v1, s37
	v_bfe_u32 v38, v39, 16, 1
	v_lshrrev_b32_e32 v1, 16, v1
	v_add3_u32 v38, v39, v38, s37
	v_and_or_b32 v38, v38, s33, v1
	v_pk_mul_f32 v[26:27], v[148:149], v[42:43]
	v_pk_fma_f32 v[18:19], v[26:27], v[34:35], v[136:137]
	v_cvt_pk_bf16_f32 v39, v40, v41
	v_bfe_u32 v1, v19, 16, 1
	v_pk_add_f32 v[40:41], v[158:159], 1.0 op_sel_hi:[1,0]
	v_add3_u32 v1, v19, v1, s37
	v_bfe_u32 v19, v18, 16, 1
	v_pk_mul_f32 v[28:29], v[150:151], v[40:41]
	v_add3_u32 v18, v18, v19, s37
	v_pk_fma_f32 v[20:21], v[28:29], v[36:37], v[138:139]
	v_lshrrev_b32_e32 v18, 16, v18
	v_and_or_b32 v40, v1, s33, v18
	v_cvt_pk_bf16_f32 v41, v20, v21
	v_lshl_add_u64 v[18:19], v[70:71], 0, s[14:15]
	global_store_dwordx4 v[18:19], v[38:41], off
	global_load_dwordx4 v[136:139], v106, s[2:3] offset:16
	global_load_dwordx4 v[140:143], v106, s[2:3]
	global_load_dwordx4 v[148:151], v[66:67], off offset:16
	global_load_dwordx4 v[152:155], v[66:67], off
	global_load_dwordx4 v[156:159], v106, s[16:17] offset:16
	global_load_dwordx4 v[160:163], v106, s[16:17]
	s_nop 0
	s_waitcnt vmcnt(13)
	v_pk_add_f32 v[20:21], v[190:191], 1.0 op_sel_hi:[1,0]
	v_pk_add_f32 v[50:51], v[188:189], 1.0 op_sel_hi:[1,0]
	v_pk_mul_f32 v[20:21], v[178:179], v[20:21]
	v_pk_mul_f32 v[42:43], v[176:177], v[50:51]
	v_pk_fma_f32 v[32:33], v[20:21], v[32:33], v[170:171]
	v_pk_fma_f32 v[20:21], v[42:43], v[30:31], v[168:169]
	v_pk_add_f32 v[30:31], v[186:187], 1.0 op_sel_hi:[1,0]
	v_bfe_u32 v1, v20, 16, 1
	v_add3_u32 v1, v20, v1, s37
	v_bfe_u32 v20, v21, 16, 1
	v_lshrrev_b32_e32 v1, 16, v1
	v_add3_u32 v20, v21, v20, s37
	v_and_or_b32 v20, v20, s33, v1
	v_bfe_u32 v1, v32, 16, 1
	v_bfe_u32 v21, v33, 16, 1
	v_add3_u32 v1, v32, v1, s37
	v_add3_u32 v21, v33, v21, s37
	v_pk_add_f32 v[32:33], v[184:185], 1.0 op_sel_hi:[1,0]
	v_lshrrev_b32_e32 v1, 16, v1
	v_pk_mul_f32 v[32:33], v[172:173], v[32:33]
	v_and_or_b32 v21, v21, s33, v1
	v_pk_fma_f32 v[22:23], v[22:23], v[32:33], v[164:165]
	v_pk_mul_f32 v[30:31], v[174:175], v[30:31]
	v_bfe_u32 v1, v23, 16, 1
	v_add3_u32 v1, v23, v1, s37
	v_bfe_u32 v23, v22, 16, 1
	v_pk_fma_f32 v[24:25], v[24:25], v[30:31], v[166:167]
	v_add3_u32 v22, v22, v23, s37
	v_lshrrev_b32_e32 v22, 16, v22
	v_and_or_b32 v22, v1, s33, v22
	v_cvt_pk_bf16_f32 v23, v24, v25
	global_store_dwordx4 v[18:19], v[20:23], off offset:1024
	s_nop 0
	s_waitcnt vmcnt(8)
	v_pk_add_f32 v[40:41], v[244:245], 1.0 op_sel_hi:[1,0]
	s_nop 0
	v_pk_mul_f32 v[32:33], v[204:205], v[40:41]
	v_pk_add_f32 v[42:43], v[246:247], 1.0 op_sel_hi:[1,0]
	v_pk_fma_f32 v[14:15], v[14:15], v[32:33], v[196:197]
	v_pk_mul_f32 v[34:35], v[206:207], v[42:43]
	v_bfe_u32 v1, v14, 16, 1
	v_add3_u32 v1, v14, v1, s37
	v_bfe_u32 v14, v15, 16, 1
	v_pk_fma_f32 v[16:17], v[16:17], v[34:35], v[198:199]
	v_lshrrev_b32_e32 v1, 16, v1
	v_add3_u32 v14, v15, v14, s37
	v_and_or_b32 v14, v14, s33, v1
	v_pk_add_f32 v[24:25], v[240:241], 1.0 op_sel_hi:[1,0]
	v_pk_mul_f32 v[24:25], v[200:201], v[24:25]
	v_pk_fma_f32 v[10:11], v[10:11], v[24:25], v[192:193]
	v_cvt_pk_bf16_f32 v15, v16, v17
	v_bfe_u32 v1, v11, 16, 1
	v_pk_add_f32 v[16:17], v[242:243], 1.0 op_sel_hi:[1,0]
	v_add3_u32 v1, v11, v1, s37
	v_bfe_u32 v11, v10, 16, 1
	v_pk_mul_f32 v[16:17], v[202:203], v[16:17]
	v_add3_u32 v10, v10, v11, s37
	v_pk_fma_f32 v[12:13], v[12:13], v[16:17], v[194:195]
	v_lshrrev_b32_e32 v10, 16, v10
	v_and_or_b32 v16, v1, s33, v10
	v_cvt_pk_bf16_f32 v17, v12, v13
	global_store_dwordx4 v[18:19], v[14:17], off offset:2048
	s_nop 0
	s_waitcnt vmcnt(2)
	v_pk_add_f32 v[32:33], v[160:161], 1.0 op_sel_hi:[1,0]
	s_nop 0
	v_pk_mul_f32 v[24:25], v[152:153], v[32:33]
	v_pk_add_f32 v[34:35], v[162:163], 1.0 op_sel_hi:[1,0]
	v_pk_fma_f32 v[6:7], v[6:7], v[24:25], v[140:141]
	v_pk_mul_f32 v[26:27], v[154:155], v[34:35]
	v_bfe_u32 v1, v6, 16, 1
	v_add3_u32 v1, v6, v1, s37
	v_bfe_u32 v6, v7, 16, 1
	v_pk_fma_f32 v[8:9], v[8:9], v[26:27], v[142:143]
	v_lshrrev_b32_e32 v1, 16, v1
	v_add3_u32 v6, v7, v6, s37
	v_and_or_b32 v6, v6, s33, v1
	v_pk_add_f32 v[14:15], v[156:157], 1.0 op_sel_hi:[1,0]
	v_pk_mul_f32 v[14:15], v[148:149], v[14:15]
	v_pk_fma_f32 v[2:3], v[2:3], v[14:15], v[136:137]
	v_cvt_pk_bf16_f32 v7, v8, v9
	v_bfe_u32 v1, v3, 16, 1
	v_pk_add_f32 v[8:9], v[158:159], 1.0 op_sel_hi:[1,0]
	v_add3_u32 v1, v3, v1, s37
	v_bfe_u32 v3, v2, 16, 1
	v_pk_mul_f32 v[8:9], v[150:151], v[8:9]
	v_add3_u32 v2, v2, v3, s37
	v_pk_fma_f32 v[4:5], v[4:5], v[8:9], v[138:139]
	v_lshrrev_b32_e32 v2, 16, v2
	v_and_or_b32 v8, v1, s33, v2
	v_cvt_pk_bf16_f32 v9, v4, v5
	global_store_dwordx4 v[18:19], v[6:9], off offset:3072
	s_branch .LBB0_2727
